# P1: converter workgroups per XCD 12 -> 10, on top of v63 (compare with 11)
# baseline (speedup 1.0000x reference)
; #define F8_LD(v, s_, d_, ok) do { ok = it < NEXP; if (ok) { f8_item(p, it, s_, d_); f8_tile_load(s_, v, lane); } it += stride; } while (0)
; __device__ __forceinline__ void f8_item(const Params& p, int it, const float*& src, unsigned char*& dst) {
;     const int which = it >> 15, r = it & 32767, e = r >> 10, q = r & 1023, kb = q >> 6, nb = q & 63;
;     if (which == 2) { src = p.w_down + (size_t)e * FF * D + (size_t)(kb * 128) * D + nb * 32; dst = p.ws + WS_WD + ((size_t)e * D + nb * 32) * 2048 + kb * 128; }
;     else { const int f0 = nb * 32, drow = (f0 >> 7) * 256 + which * 128 + (f0 & 127);
;         src = (which == 0 ? p.w_gate : p.w_up) + (size_t)e * D * FF + (size_t)(kb * 128) * FF + f0; dst = p.ws + WS_WGU + ((size_t)e * 4096 + drow) * 2048 + kb * 128; }
; }
; __device__ __forceinline__ void convert_experts(const Params& p, int first, int stride, int lane) {
;     constexpr int NEXP = 3 * NE * 1024;
;     f32x4 va[16], vb[16], vc[16]; const float* sa; unsigned char* da; const float* sb; unsigned char* db; const float* sc; unsigned char* dc;
;     int it = first; bool oka, okb, okc;
;     ...
;     F8_LD(va, sa, da, oka); F8_LD(vb, sb, db, okb); F8_LD(vc, sc, dc, okc);
; __global__ void __launch_bounds__(NTHREADS, 2) hymba_fwd(Params p) {
;     ...
;         const int ncw = (G < 8 * NCV) ? G : 8 * NCV;
;         if (cid < ncw) convert_experts(p, cid * NWAVES + wave, ncw * NWAVES, lane);
.LBB0_146:
	s_load_dwordx16 s[12:27], s[0:1], 0x80
	s_cmp_lt_i32 s48, 2
	s_cselect_b64 s[4:5], -1, 0
	s_and_b64 s[0:1], s[4:5], s[10:11]
	s_andn2_b64 vcc, exec, s[0:1]
	s_waitcnt lgkmcnt(0)
	v_writelane_b32 v255, s12, 29
	s_mov_b32 s0, s90
	s_nop 0
	v_writelane_b32 v255, s13, 30
	v_writelane_b32 v255, s14, 31
	v_writelane_b32 v255, s15, 32
	v_writelane_b32 v255, s16, 33
	v_writelane_b32 v255, s17, 34
	v_writelane_b32 v255, s18, 35
	v_writelane_b32 v255, s19, 36
	v_writelane_b32 v255, s20, 37
	v_writelane_b32 v255, s21, 38
	v_writelane_b32 v255, s22, 39
	v_writelane_b32 v255, s23, 40
	v_writelane_b32 v255, s24, 41
	v_writelane_b32 v255, s25, 42
	v_writelane_b32 v255, s26, 43
	v_writelane_b32 v255, s27, 44
	v_writelane_b32 v255, s0, 45
	s_nop 1
	v_writelane_b32 v255, s1, 46
	s_mov_b32 s0, s68
	v_writelane_b32 v255, s0, 47
	s_nop 1
	v_writelane_b32 v255, s1, 48
	s_cbranch_vccnz .LBB0_224
	s_min_i32 s27, s96, 0x50
	v_readlane_b32 s0, v255, 28
	s_cmp_ge_i32 s0, s27
	s_cbranch_scc1 .LBB0_192
	v_readlane_b32 s0, v255, 28
	s_lshl_b32 s0, s0, 3
	v_readlane_b32 s6, v255, 22
	s_add_i32 s2, s0, s6
	s_cmp_lt_i32 s2, 0x18000
	s_cselect_b64 s[14:15], -1, 0
	s_cmp_gt_i32 s2, 0x17fff
	v_readlane_b32 s7, v255, 23
	s_cbranch_scc1 .LBB0_151
	s_ashr_i32 s0, s2, 15
	s_bfe_u32 s10, s2, 0x5000a
	s_bfe_u32 s12, s2, 0x40006
	s_and_b32 s11, s2, 63
	s_cmp_lg_u32 s0, 2
	s_cbranch_scc0 .LBB0_152
	s_lshl_b32 s6, s11, 6
	s_lshl_b32 s1, s11, 5
	s_and_b32 s6, s6, 0xf00
	s_lshl_b32 s0, s0, 7
	s_add_i32 s6, s6, s0
	s_and_b32 s0, s1, 0x60
	s_or_b32 s0, s6, s0
	v_readlane_b32 s52, v255, 29
	s_cmpk_lt_u32 s2, 0x8000
	v_readlane_b32 s54, v255, 31
	v_readlane_b32 s55, v255, 32
	v_readlane_b32 s58, v255, 35
	v_readlane_b32 s59, v255, 36
	s_cselect_b32 s1, s55, s59
	s_cselect_b32 s6, s54, s58
	s_lshl_b32 s7, s10, 24
	s_add_u32 s6, s6, s7
	s_addc_u32 s1, s1, 0
	s_lshl_b32 s8, s12, 7
	s_lshl_b32 s7, s12, 20
	s_add_u32 s6, s6, s7
	s_addc_u32 s1, s1, 0
	s_lshl_b32 s7, s11, 7
	s_add_u32 s6, s6, s7
	s_addc_u32 s7, s1, 0
	s_ashr_i32 s1, s0, 31
	s_lshl_b32 s9, s10, 23
	s_lshl_b64 s[0:1], s[0:1], 11
	s_add_u32 s9, s88, s9
	s_addc_u32 s13, s89, 0
	s_add_u32 s0, s9, s0
	s_addc_u32 s1, s13, s1
	s_add_u32 s0, s0, s8
	s_addc_u32 s1, s1, 0
	s_add_u32 s0, s0, 0x1000000
	v_readlane_b32 s53, v255, 30
	v_readlane_b32 s56, v255, 33
	v_readlane_b32 s57, v255, 34
	v_readlane_b32 s60, v255, 37
	v_readlane_b32 s61, v255, 38
	v_readlane_b32 s62, v255, 39
	v_readlane_b32 s63, v255, 40
	v_readlane_b32 s64, v255, 41
	v_readlane_b32 s65, v255, 42
	v_readlane_b32 s66, v255, 43
	v_readlane_b32 s67, v255, 44
	s_addc_u32 s1, s1, 0
	s_cbranch_execz .LBB0_153
	s_branch .LBB0_154
